# speedup vs baseline: 1.0357x; 1.0357x over previous
_Z12giou_partialPK15HIP_vector_typeIfLj4EES2_S2_PKiPS_IfLj2EE:
	s_setprio 3
	s_load_dwordx8 s[16:23], s[0:1], 0x0
	s_load_dwordx2 s[24:25], s[0:1], 0x20
	s_movk_i32 s3, 0x200
	s_lshl_b32 s6, s2, 9
	v_cmp_gt_u32_e32 vcc, s3, v0
	v_lshlrev_b32_e32 v11, 4, v0
	v_lshrrev_b32_e32 v1, 6, v0
	v_and_b32_e32 v10, 63, v0
	v_lshl_add_u32 v6, v1, 18, s6
	v_lshlrev_b32_e32 v8, 2, v6
	v_lshl_add_u32 v8, v10, 4, v8
	s_lshl_b32 s7, s2, 13
	v_readfirstlane_b32 s15, v1
	s_waitcnt lgkmcnt(0)
	s_add_u32 s20, s20, s7
	s_addc_u32 s21, s21, 0
	global_load_dwordx4 v[12:15], v8, s[22:23] nt
	global_load_dwordx4 v[16:19], v8, s[22:23] offset:1024 nt
	s_and_saveexec_b64 s[8:9], vcc
	s_cbranch_execz .Lno_anc
	global_load_dwordx4 v[2:5], v11, s[20:21] nt
.Lno_anc:
	s_or_b64 exec, exec, s[8:9]
	s_setprio 0
	v_mov_b32_e32 v7, 0x80
	s_and_b32 s27, s2, 0xf8
	s_cmp_lg_u32 s27, 0
	s_cbranch_scc1 .Lno_touch
	v_lshlrev_b32_e32 v9, 4, v6
	s_mov_b64 exec, 1
	global_load_dword v24, v9, s[16:17] nt
	global_load_dword v25, v9, s[18:19] nt
	s_mov_b64 exec, -1
	s_waitcnt vmcnt(2)
	s_branch .Lmask_ready
